# E(0) rows: discarded y/select/residual-update work skipped (register permutation of the f32 row instead)
# speedup vs baseline: 1.0258x; 1.0018x over previous
; __device__ __forceinline__ float h_lo(unsigned u) { return (float)__builtin_bit_cast(f16v2, u)[0]; }
; __device__ __forceinline__ float h_hi(unsigned u) { return (float)__builtin_bit_cast(f16v2, u)[1]; }
; __device__ __forceinline__ float lo16(unsigned u) { return __uint_as_float(u << 16); }
; __device__ __forceinline__ float hi16(unsigned u) { return __uint_as_float(u & 0xffff0000u); }
; __device__ void phase_E_rows(const Params& p, int l, char* smem, int vb, int nvb, bool split, int nrows, int oz) {
;     ...
;         float4 xv[4];
;         u32x4 yq[2];
; #pragma unroll
;         for (int k = 0; k < 4; ++k) {
;             const u32x4 w = nxb0[k >> 1];
;             const int h2 = 2 * (k & 1);
;             xv[k] = (l <= 1) ? nx0[k] : make_float4(h_lo(w[h2]), h_hi(w[h2]), h_lo(w[h2 + 1]), h_hi(w[h2 + 1]));
;         }
; #pragma unroll
;         for (int k = 0; k < 4; ++k) nx0[k] = nx1[k];
; #pragma unroll
;         for (int k2 = 0; k2 < 2; ++k2) { yq[k2] = ny0[k2]; nxb0[k2] = nxb1[k2]; ny0[k2] = ny1[k2]; }
;         if (row + 2 < rend) E2_LOAD(nx1, nxb1, ny1, row + 2)
;         float y[4][4];
;         float ss = 0.f;
; #pragma unroll
;         for (int k = 0; k < 4; ++k) {
;             { const u32x4 w = yq[k >> 1]; const int h2 = 2 * (k & 1); y[k][0] = lo16(w[h2]); y[k][1] = hi16(w[h2]); y[k][2] = lo16(w[h2 + 1]); y[k][3] = hi16(w[h2 + 1]); }
;             ss += y[k][0] * y[k][0] + y[k][1] * y[k][1] + y[k][2] * y[k][2] + y[k][3] * y[k][3];
;         }
;         float rs = 0.f;
;         if (l > 0) {
;             ss = wave_sum(ss);
;             rs = rsqrtf(ss * (1.f / DM) + EPS);
;         }
;         float ss2 = 0.f;
; #pragma unroll
;         for (int k = 0; k < 4; ++k) {
;             if (l > 0) {
;                 xv[k].x += gp[k].x * (y[k][0] * rs);
;                 xv[k].y += gp[k].y * (y[k][1] * rs);
;                 xv[k].z += gp[k].z * (y[k][2] * rs);
;                 xv[k].w += gp[k].w * (y[k][3] * rs);
;             }
;             ss2 += xv[k].x * xv[k].x + xv[k].y * xv[k].y + xv[k].z * xv[k].z + xv[k].w * xv[k].w;
;         }
.LBB0_957:
	s_and_b64 vcc, exec, s[44:45]
	s_cbranch_vccz .Le0_full
	v_mov_b64_e32 v[20:21], v[42:43]
	v_mov_b64_e32 v[22:23], v[38:39]
	v_mov_b64_e32 v[24:25], v[34:35]
	v_mov_b64_e32 v[26:27], v[40:41]
	v_mov_b64_e32 v[176:177], v[28:29]
	v_mov_b64_e32 v[28:29], v[30:31]
	v_mov_b64_e32 v[30:31], v[36:37]
	v_mov_b64_e32 v[34:35], v[176:177]
	s_branch .LBB0_962
